# conversion routine reads the two weight pointers from frame lanes (loaded once at entry) instead of an s_load + wait per call
# baseline (speedup 1.0000x reference)
_Z8mega_fwd4Args:
	s_load_dwordx2 s[18:19], s[0:1], 0xb0
	s_load_dword s92, s[0:1], 0xc0
	s_mov_b32 s94, s2
	s_add_u32 s2, s0, 0xc0
	s_addc_u32 s3, s1, 0
	v_readfirstlane_b32 s58, v0
	v_writelane_b32 v252, s2, 0
	v_cmp_gt_u32_e32 vcc, 64, v0
	s_nop 0
	v_writelane_b32 v252, s3, 1
	s_and_saveexec_b64 s[2:3], vcc
	v_lshl_add_u32 v1, v0, 2, 0
	v_add_u32_e32 v1, 0x26400, v1
	v_mov_b32_e32 v2, 0
	ds_write_b32 v1, v2
	s_or_b64 exec, exec, s[2:3]
	s_load_dwordx2 s[88:89], s[0:1], 0xb8
	s_load_dwordx2 s[20:21], s[0:1], 0x78
	s_load_dwordx2 s[22:23], s[0:1], 0x88
	s_waitcnt lgkmcnt(0)
	v_writelane_b32 v255, s94, 0
	v_writelane_b32 v255, s58, 1
	v_writelane_b32 v255, 0, 2
	v_writelane_b32 v255, 0, 3
	v_writelane_b32 v255, s92, 4
	v_writelane_b32 v255, s0, 7
	v_writelane_b32 v255, s1, 8
	v_writelane_b32 v255, s18, 9
	v_writelane_b32 v255, s19, 10
	v_writelane_b32 v255, s20, 11
	v_writelane_b32 v255, s21, 12
	v_writelane_b32 v255, s22, 13
	v_writelane_b32 v255, s23, 14
	s_add_u32 s2, s18, 0x4000
	s_addc_u32 s3, s19, 0
	v_writelane_b32 v252, s2, 2
	s_mov_b32 s87, 0
	s_nop 0
	v_writelane_b32 v252, s3, 3
	s_sub_i32 s2, s89, s88
	s_cmp_lt_i32 s2, 2
	s_mov_b32 s2, 0
	s_barrier
	s_cbranch_scc1 .LBB0_7
	s_getreg_b32 s2, hwreg(HW_REG_XCC_ID, 0, 4)
	s_and_b32 s87, s2, 15
	v_cmp_eq_u32_e32 vcc, 0, v0
	s_and_saveexec_b64 s[2:3], vcc
	s_cbranch_execz .LBB0_6
	s_mov_b64 s[4:5], exec
	v_mbcnt_lo_u32_b32 v1, s4, 0
	v_mbcnt_hi_u32_b32 v1, s5, v1
	v_cmp_eq_u32_e32 vcc, 0, v1
	s_and_b64 s[6:7], exec, vcc
	s_mov_b64 exec, s[6:7]
	s_cbranch_execz .LBB0_6
	s_bcnt1_i32_b64 s4, s[4:5]
	s_lshl_b32 s6, s87, 8
	v_mov_b32_e32 v2, s4
	v_readlane_b32 s4, v252, 2
	v_mov_b32_e32 v1, s6
	v_readlane_b32 s5, v252, 3
	s_nop 4
	global_atomic_add v1, v2, s[4:5] offset:1024

.Lmy_cvgu:
	v_writelane_b32 v254, s20, 0
	v_writelane_b32 v254, s21, 1
	v_writelane_b32 v254, s22, 2
	v_writelane_b32 v254, s23, 3
	v_writelane_b32 v254, s24, 4
	v_writelane_b32 v254, s25, 5
	v_writelane_b32 v254, s26, 6
	v_writelane_b32 v254, s27, 7
	v_writelane_b32 v254, s28, 8
	v_writelane_b32 v254, s29, 9
	v_writelane_b32 v254, s30, 10
	v_writelane_b32 v254, s31, 11
	v_writelane_b32 v254, s32, 12
	v_writelane_b32 v254, s33, 13
	v_writelane_b32 v254, s34, 14
	v_writelane_b32 v254, s35, 15
	v_writelane_b32 v254, s36, 16
	v_writelane_b32 v254, s37, 17
	v_writelane_b32 v254, s38, 18
	v_writelane_b32 v254, s39, 19
	v_writelane_b32 v254, s40, 20
	v_writelane_b32 v254, s41, 21
	v_writelane_b32 v254, s42, 22
	v_writelane_b32 v254, s43, 23
	v_writelane_b32 v254, s44, 24
	v_writelane_b32 v254, s45, 25
	v_writelane_b32 v254, s46, 26
	v_writelane_b32 v254, s47, 27
	v_writelane_b32 v254, s48, 28
	v_writelane_b32 v254, s49, 29
	v_writelane_b32 v254, s50, 30
	v_writelane_b32 v254, s51, 31
	v_readlane_b32 s44, v255, 0
	v_readlane_b32 s45, v255, 1
	v_readlane_b32 s27, v255, 2
	v_readlane_b32 s47, v255, 4
	v_readlane_b32 s24, v255, 6
	v_readlane_b32 s48, v255, 7
	v_readlane_b32 s49, v255, 8
	v_readlane_b32 s30, v255, 9
	v_readlane_b32 s31, v255, 10
	s_nop 4
	v_readlane_b32 s28, v255, 11
	v_readlane_b32 s29, v255, 12
	s_nop 4
	s_add_u32 s30, s30, 0x2d800000
	s_addc_u32 s31, s31, 0
	s_mov_b32 s20, 0x42800000
	s_mov_b32 s21, 0x42800000
	s_lshr_b32 s22, s47, 2
	s_lshl_b32 s22, s22, 3
	s_lshr_b32 s50, s44, 3
	s_and_b32 s50, s50, 3
	s_add_i32 s23, s50, 1
	s_lshl_b32 s23, s23, 14
	s_lshl_b32 s50, s50, 14
	s_lshr_b32 s51, s44, 5
	s_lshl_b32 s51, s51, 3
	s_and_b32 s44, s44, 7
	s_or_b32 s51, s51, s44
	s_lshl_b32 s51, s51, 3
	s_lshr_b32 s45, s45, 6
	s_add_i32 s51, s51, s45
	s_add_i32 s51, s51, s50
	s_mul_i32 s25, s27, s22
	s_add_i32 s25, s25, s51
	s_add_i32 s26, s25, s22
	s_lshr_b32 s24, s24, 1
	v_mbcnt_lo_u32_b32 v66, -1, 0
	v_mbcnt_hi_u32_b32 v66, -1, v66
	v_and_b32_e32 v132, 7, v66
	v_lshrrev_b32_e32 v134, 3, v66
	v_lshlrev_b32_e32 v64, 18, v134
	v_lshl_or_b32 v64, v132, 4, v64
	v_lshlrev_b32_e32 v65, 12, v134
	v_lshl_or_b32 v65, v132, 4, v65
	v_lshlrev_b32_e32 v66, 5, v132
	v_lshl_or_b32 v66, v134, 2, v66
	s_cmp_eq_u32 s24, 0
	s_cbranch_scc1 .Lmy_cvgu_done
	s_cmp_ge_i32 s26, s23
	s_cbranch_scc1 .Lmy_cvgu_done
	s_waitcnt lgkmcnt(0)
	s_lshr_b32 s44, s25, 7
	s_lshl_b32 s44, s44, 21
	s_and_b32 s45, s25, 127
	s_lshl_b32 s45, s45, 7
	s_add_u32 s44, s44, s45
	s_add_u32 s32, s28, s44
	s_addc_u32 s33, s29, 0
	s_lshr_b32 s44, s25, 11
	s_lshl_b32 s44, s44, 23
	s_and_b32 s45, s25, 127
	s_lshr_b32 s46, s45, 3
	s_lshl_b32 s46, s46, 19
	s_and_b32 s45, s45, 7
	s_lshl_b32 s45, s45, 15
	s_bfe_u32 s47, s25, 0x40007
	s_lshl_b32 s47, s47, 7
	s_add_u32 s44, s44, s46
	s_add_u32 s45, s45, s47
	s_add_u32 s44, s44, s45
	s_add_u32 s34, s30, s44
	s_addc_u32 s35, s31, 0
	s_lshr_b32 s44, s26, 7
	s_lshl_b32 s44, s44, 21
	s_and_b32 s45, s26, 127
	s_lshl_b32 s45, s45, 7
	s_add_u32 s44, s44, s45
	s_add_u32 s36, s28, s44
	s_addc_u32 s37, s29, 0
	s_lshr_b32 s44, s26, 11
	s_lshl_b32 s44, s44, 23
	s_and_b32 s45, s26, 127
	s_lshr_b32 s46, s45, 3
	s_lshl_b32 s46, s46, 19
	s_and_b32 s45, s45, 7
	s_lshl_b32 s45, s45, 15
	s_bfe_u32 s47, s26, 0x40007
	s_lshl_b32 s47, s47, 7
	s_add_u32 s44, s44, s46
	s_add_u32 s45, s45, s47
	s_add_u32 s44, s44, s45
	s_add_u32 s38, s30, s44
	s_addc_u32 s39, s31, 0
	global_load_dwordx4 v[4:7], v64, s[32:33] nt
	s_add_u32 s40, s32, 0x4000
	s_addc_u32 s41, s33, 0
	global_load_dwordx4 v[8:11], v64, s[40:41] nt
	s_add_u32 s40, s32, 0x8000
	s_addc_u32 s41, s33, 0
	global_load_dwordx4 v[12:15], v64, s[40:41] nt
	s_add_u32 s40, s32, 0xc000
	s_addc_u32 s41, s33, 0
	global_load_dwordx4 v[16:19], v64, s[40:41] nt
	s_add_u32 s40, s32, 0x10000
	s_addc_u32 s41, s33, 0
	global_load_dwordx4 v[20:23], v64, s[40:41] nt
	s_add_u32 s40, s32, 0x14000
	s_addc_u32 s41, s33, 0
	global_load_dwordx4 v[24:27], v64, s[40:41] nt
	s_add_u32 s40, s32, 0x18000
	s_addc_u32 s41, s33, 0
	global_load_dwordx4 v[28:31], v64, s[40:41] nt
	s_add_u32 s40, s32, 0x1c000
	s_addc_u32 s41, s33, 0
	global_load_dwordx4 v[32:35], v64, s[40:41] nt
	s_add_u32 s40, s32, 0x20000
	s_addc_u32 s41, s33, 0
	global_load_dwordx4 v[36:39], v64, s[40:41] nt
	s_add_u32 s40, s32, 0x24000
	s_addc_u32 s41, s33, 0
	global_load_dwordx4 v[40:43], v64, s[40:41] nt
	s_add_u32 s40, s32, 0x28000
	s_addc_u32 s41, s33, 0
	global_load_dwordx4 v[44:47], v64, s[40:41] nt
	s_add_u32 s40, s32, 0x2c000
	s_addc_u32 s41, s33, 0
	global_load_dwordx4 v[48:51], v64, s[40:41] nt
	s_add_u32 s40, s32, 0x30000
	s_addc_u32 s41, s33, 0
	global_load_dwordx4 v[52:55], v64, s[40:41] nt
	s_add_u32 s40, s32, 0x34000
	s_addc_u32 s41, s33, 0
	global_load_dwordx4 v[56:59], v64, s[40:41] nt
	s_add_u32 s40, s32, 0x38000
	s_addc_u32 s41, s33, 0
	global_load_dwordx4 v[60:63], v64, s[40:41] nt
	s_add_u32 s40, s32, 0x3c000
	s_addc_u32 s41, s33, 0
	global_load_dwordx4 v[138:141], v64, s[40:41] nt
	global_load_dwordx4 v[68:71], v64, s[36:37] nt
	s_add_u32 s40, s36, 0x4000
	s_addc_u32 s41, s37, 0
	global_load_dwordx4 v[72:75], v64, s[40:41] nt
	s_add_u32 s40, s36, 0x8000
	s_addc_u32 s41, s37, 0
	global_load_dwordx4 v[76:79], v64, s[40:41] nt
	s_add_u32 s40, s36, 0xc000
	s_addc_u32 s41, s37, 0
	global_load_dwordx4 v[80:83], v64, s[40:41] nt
	s_add_u32 s40, s36, 0x10000
	s_addc_u32 s41, s37, 0
	global_load_dwordx4 v[84:87], v64, s[40:41] nt
	s_add_u32 s40, s36, 0x14000
	s_addc_u32 s41, s37, 0
	global_load_dwordx4 v[88:91], v64, s[40:41] nt
	s_add_u32 s40, s36, 0x18000
	s_addc_u32 s41, s37, 0
	global_load_dwordx4 v[92:95], v64, s[40:41] nt
	s_add_u32 s40, s36, 0x1c000
	s_addc_u32 s41, s37, 0
	global_load_dwordx4 v[96:99], v64, s[40:41] nt
	s_add_u32 s40, s36, 0x20000
	s_addc_u32 s41, s37, 0
	global_load_dwordx4 v[100:103], v64, s[40:41] nt
	s_add_u32 s40, s36, 0x24000
	s_addc_u32 s41, s37, 0
	global_load_dwordx4 v[104:107], v64, s[40:41] nt
	s_add_u32 s40, s36, 0x28000
	s_addc_u32 s41, s37, 0
	global_load_dwordx4 v[108:111], v64, s[40:41] nt
	s_add_u32 s40, s36, 0x2c000
	s_addc_u32 s41, s37, 0
	global_load_dwordx4 v[112:115], v64, s[40:41] nt
	s_add_u32 s40, s36, 0x30000
	s_addc_u32 s41, s37, 0
	global_load_dwordx4 v[116:119], v64, s[40:41] nt
	s_add_u32 s40, s36, 0x34000
	s_addc_u32 s41, s37, 0
	global_load_dwordx4 v[120:123], v64, s[40:41] nt
	s_add_u32 s40, s36, 0x38000
	s_addc_u32 s41, s37, 0
	global_load_dwordx4 v[124:127], v64, s[40:41] nt
	s_add_u32 s40, s36, 0x3c000
	s_addc_u32 s41, s37, 0
	global_load_dwordx4 v[128:131], v64, s[40:41] nt
	s_sub_u32 s24, s24, 1
	s_add_i32 s27, s27, 2
	s_waitcnt vmcnt(16)

.Lmy_cvdn:
	v_writelane_b32 v254, s20, 0
	v_writelane_b32 v254, s21, 1
	v_writelane_b32 v254, s22, 2
	v_writelane_b32 v254, s23, 3
	v_writelane_b32 v254, s24, 4
	v_writelane_b32 v254, s25, 5
	v_writelane_b32 v254, s26, 6
	v_writelane_b32 v254, s27, 7
	v_writelane_b32 v254, s28, 8
	v_writelane_b32 v254, s29, 9
	v_writelane_b32 v254, s30, 10
	v_writelane_b32 v254, s31, 11
	v_writelane_b32 v254, s32, 12
	v_writelane_b32 v254, s33, 13
	v_writelane_b32 v254, s34, 14
	v_writelane_b32 v254, s35, 15
	v_writelane_b32 v254, s36, 16
	v_writelane_b32 v254, s37, 17
	v_writelane_b32 v254, s38, 18
	v_writelane_b32 v254, s39, 19
	v_writelane_b32 v254, s40, 20
	v_writelane_b32 v254, s41, 21
	v_writelane_b32 v254, s42, 22
	v_writelane_b32 v254, s43, 23
	v_writelane_b32 v254, s44, 24
	v_writelane_b32 v254, s45, 25
	v_writelane_b32 v254, s46, 26
	v_writelane_b32 v254, s47, 27
	v_writelane_b32 v254, s48, 28
	v_writelane_b32 v254, s49, 29
	v_writelane_b32 v254, s50, 30
	v_writelane_b32 v254, s51, 31
	v_readlane_b32 s44, v255, 0
	v_readlane_b32 s45, v255, 1
	v_readlane_b32 s27, v255, 3
	v_readlane_b32 s47, v255, 4
	v_readlane_b32 s24, v255, 6
	v_readlane_b32 s48, v255, 7
	v_readlane_b32 s49, v255, 8
	v_readlane_b32 s30, v255, 9
	v_readlane_b32 s31, v255, 10
	s_nop 4
	v_readlane_b32 s28, v255, 13
	v_readlane_b32 s29, v255, 14
	s_nop 4
	s_add_u32 s30, s30, 0x4d800000
	s_addc_u32 s31, s31, 0
	s_mov_b32 s20, 0x42800000
	s_mov_b32 s21, 0x42800000
	s_lshr_b32 s22, s47, 2
	s_lshl_b32 s22, s22, 3
	s_lshr_b32 s50, s44, 3
	s_and_b32 s50, s50, 3
	s_add_i32 s23, s50, 1
	s_lshl_b32 s23, s23, 13
	s_lshl_b32 s50, s50, 13
	s_lshr_b32 s51, s44, 5
	s_lshl_b32 s51, s51, 3
	s_and_b32 s44, s44, 7
	s_or_b32 s51, s51, s44
	s_lshl_b32 s51, s51, 3
	s_lshr_b32 s45, s45, 6
	s_add_i32 s51, s51, s45
	s_add_i32 s51, s51, s50
	s_mul_i32 s25, s27, s22
	s_add_i32 s25, s25, s51
	s_add_i32 s26, s25, s22
	s_lshr_b32 s24, s24, 1
	v_mbcnt_lo_u32_b32 v66, -1, 0
	v_mbcnt_hi_u32_b32 v66, -1, v66
	v_and_b32_e32 v132, 7, v66
	v_lshrrev_b32_e32 v134, 3, v66
	v_lshlrev_b32_e32 v64, 17, v134
	v_lshl_or_b32 v64, v132, 4, v64
	v_lshlrev_b32_e32 v65, 13, v134
	v_lshl_or_b32 v65, v132, 4, v65
	v_lshlrev_b32_e32 v66, 5, v132
	v_lshl_or_b32 v66, v134, 2, v66
	s_cmp_eq_u32 s24, 0
	s_cbranch_scc1 .Lmy_cvdn_done
	s_cmp_ge_i32 s26, s23
	s_cbranch_scc1 .Lmy_cvdn_done
	s_waitcnt lgkmcnt(0)
	s_lshr_b32 s44, s25, 6
	s_lshl_b32 s44, s44, 20
	s_and_b32 s45, s25, 63
	s_lshl_b32 s45, s45, 7
	s_add_u32 s44, s44, s45
	s_add_u32 s32, s28, s44
	s_addc_u32 s33, s29, 0
	s_lshr_b32 s44, s25, 10
	s_lshl_b32 s44, s44, 22
	s_and_b32 s45, s25, 63
	s_lshl_b32 s45, s45, 16
	s_bfe_u32 s46, s25, 0x40006
	s_lshl_b32 s46, s46, 7
	s_add_u32 s44, s44, s45
	s_add_u32 s44, s44, s46
	s_add_u32 s34, s30, s44
	s_addc_u32 s35, s31, 0
	s_lshr_b32 s44, s26, 6
	s_lshl_b32 s44, s44, 20
	s_and_b32 s45, s26, 63
	s_lshl_b32 s45, s45, 7
	s_add_u32 s44, s44, s45
	s_add_u32 s36, s28, s44
	s_addc_u32 s37, s29, 0
	s_lshr_b32 s44, s26, 10
	s_lshl_b32 s44, s44, 22
	s_and_b32 s45, s26, 63
	s_lshl_b32 s45, s45, 16
	s_bfe_u32 s46, s26, 0x40006
	s_lshl_b32 s46, s46, 7
	s_add_u32 s44, s44, s45
	s_add_u32 s44, s44, s46
	s_add_u32 s38, s30, s44
	s_addc_u32 s39, s31, 0
	global_load_dwordx4 v[4:7], v64, s[32:33] nt
	s_add_u32 s40, s32, 0x2000
	s_addc_u32 s41, s33, 0
	global_load_dwordx4 v[8:11], v64, s[40:41] nt
	s_add_u32 s40, s32, 0x4000
	s_addc_u32 s41, s33, 0
	global_load_dwordx4 v[12:15], v64, s[40:41] nt
	s_add_u32 s40, s32, 0x6000
	s_addc_u32 s41, s33, 0
	global_load_dwordx4 v[16:19], v64, s[40:41] nt
	s_add_u32 s40, s32, 0x8000
	s_addc_u32 s41, s33, 0
	global_load_dwordx4 v[20:23], v64, s[40:41] nt
	s_add_u32 s40, s32, 0xa000
	s_addc_u32 s41, s33, 0
	global_load_dwordx4 v[24:27], v64, s[40:41] nt
	s_add_u32 s40, s32, 0xc000
	s_addc_u32 s41, s33, 0
	global_load_dwordx4 v[28:31], v64, s[40:41] nt
	s_add_u32 s40, s32, 0xe000
	s_addc_u32 s41, s33, 0
	global_load_dwordx4 v[32:35], v64, s[40:41] nt
	s_add_u32 s40, s32, 0x10000
	s_addc_u32 s41, s33, 0
	global_load_dwordx4 v[36:39], v64, s[40:41] nt
	s_add_u32 s40, s32, 0x12000
	s_addc_u32 s41, s33, 0
	global_load_dwordx4 v[40:43], v64, s[40:41] nt
	s_add_u32 s40, s32, 0x14000
	s_addc_u32 s41, s33, 0
	global_load_dwordx4 v[44:47], v64, s[40:41] nt
	s_add_u32 s40, s32, 0x16000
	s_addc_u32 s41, s33, 0
	global_load_dwordx4 v[48:51], v64, s[40:41] nt
	s_add_u32 s40, s32, 0x18000
	s_addc_u32 s41, s33, 0
	global_load_dwordx4 v[52:55], v64, s[40:41] nt
	s_add_u32 s40, s32, 0x1a000
	s_addc_u32 s41, s33, 0
	global_load_dwordx4 v[56:59], v64, s[40:41] nt
	s_add_u32 s40, s32, 0x1c000
	s_addc_u32 s41, s33, 0
	global_load_dwordx4 v[60:63], v64, s[40:41] nt
	s_add_u32 s40, s32, 0x1e000
	s_addc_u32 s41, s33, 0
	global_load_dwordx4 v[138:141], v64, s[40:41] nt
	global_load_dwordx4 v[68:71], v64, s[36:37] nt
	s_add_u32 s40, s36, 0x2000
	s_addc_u32 s41, s37, 0
	global_load_dwordx4 v[72:75], v64, s[40:41] nt
	s_add_u32 s40, s36, 0x4000
	s_addc_u32 s41, s37, 0
	global_load_dwordx4 v[76:79], v64, s[40:41] nt
	s_add_u32 s40, s36, 0x6000
	s_addc_u32 s41, s37, 0
	global_load_dwordx4 v[80:83], v64, s[40:41] nt
	s_add_u32 s40, s36, 0x8000
	s_addc_u32 s41, s37, 0
	global_load_dwordx4 v[84:87], v64, s[40:41] nt
	s_add_u32 s40, s36, 0xa000
	s_addc_u32 s41, s37, 0
	global_load_dwordx4 v[88:91], v64, s[40:41] nt
	s_add_u32 s40, s36, 0xc000
	s_addc_u32 s41, s37, 0
	global_load_dwordx4 v[92:95], v64, s[40:41] nt
	s_add_u32 s40, s36, 0xe000
	s_addc_u32 s41, s37, 0
	global_load_dwordx4 v[96:99], v64, s[40:41] nt
	s_add_u32 s40, s36, 0x10000
	s_addc_u32 s41, s37, 0
	global_load_dwordx4 v[100:103], v64, s[40:41] nt
	s_add_u32 s40, s36, 0x12000
	s_addc_u32 s41, s37, 0
	global_load_dwordx4 v[104:107], v64, s[40:41] nt
	s_add_u32 s40, s36, 0x14000
	s_addc_u32 s41, s37, 0
	global_load_dwordx4 v[108:111], v64, s[40:41] nt
	s_add_u32 s40, s36, 0x16000
	s_addc_u32 s41, s37, 0
	global_load_dwordx4 v[112:115], v64, s[40:41] nt
	s_add_u32 s40, s36, 0x18000
	s_addc_u32 s41, s37, 0
	global_load_dwordx4 v[116:119], v64, s[40:41] nt
	s_add_u32 s40, s36, 0x1a000
	s_addc_u32 s41, s37, 0
	global_load_dwordx4 v[120:123], v64, s[40:41] nt
	s_add_u32 s40, s36, 0x1c000
	s_addc_u32 s41, s37, 0
	global_load_dwordx4 v[124:127], v64, s[40:41] nt
	s_add_u32 s40, s36, 0x1e000
	s_addc_u32 s41, s37, 0
	global_load_dwordx4 v[128:131], v64, s[40:41] nt
	s_sub_u32 s24, s24, 1
	s_add_i32 s27, s27, 2
	s_waitcnt vmcnt(16)
